# P11: next row's slot indices prefetched one iteration ahead
# speedup vs baseline: 1.0036x; 1.0011x over previous
.LBB0_1283:
	s_cmp_gt_i32 s56, 11
	s_cselect_b64 s[0:1], -1, 0
	s_cmp_lt_i32 s57, 12
	s_cselect_b64 s[2:3], -1, 0
	s_or_b64 s[0:1], s[0:1], s[2:3]
	s_and_b64 vcc, exec, s[0:1]
	s_cbranch_vccnz .LBB0_1287
	s_lshl_b32 s0, s94, 3
	s_add_i32 s2, s0, s91
	s_cmpk_gt_i32 s2, 0x7fff
	s_cbranch_scc1 .LBB0_1287
	s_waitcnt lgkmcnt(0)
	v_and_b32_e32 v18, 63, v0
	v_lshlrev_b32_e32 v20, 4, v18
	global_load_dwordx4 v[0:3], v20, s[80:81]
	global_load_dwordx4 v[4:7], v20, s[80:81] offset:1024
	global_load_dwordx4 v[8:11], v20, s[80:81] offset:2048
	global_load_dwordx4 v[12:15], v20, s[80:81] offset:3072
	v_mbcnt_lo_u32_b32 v19, -1, 0
	v_mbcnt_hi_u32_b32 v19, -1, v19
	v_and_b32_e32 v22, 64, v19
	v_add_u32_e32 v22, 64, v22
	v_xor_b32_e32 v23, 1, v19
	v_cmp_lt_i32_e32 vcc, v23, v22
	v_mov_b32_e32 v21, 0
	s_waitcnt vmcnt(0)
	v_lshlrev_b32_e32 v16, 2, v18
	v_cndmask_b32_e32 v23, v19, v23, vcc
	v_lshlrev_b32_e32 v30, 2, v23
	v_xor_b32_e32 v23, 2, v19
	v_cmp_lt_i32_e32 vcc, v23, v22
	v_mov_b32_e32 v17, v21
	s_lshl_b32 s4, s84, 3
	v_cndmask_b32_e32 v23, v19, v23, vcc
	v_lshlrev_b32_e32 v31, 2, v23
	v_xor_b32_e32 v23, 4, v19
	v_cmp_lt_i32_e32 vcc, v23, v22
	v_lshl_add_u64 v[16:17], s[92:93], 0, v[16:17]
	s_mov_b64 s[0:1], 0x16000000
	v_cndmask_b32_e32 v23, v19, v23, vcc
	v_lshlrev_b32_e32 v32, 2, v23
	v_xor_b32_e32 v23, 8, v19
	v_cmp_lt_i32_e32 vcc, v23, v22
	s_ashr_i32 s3, s2, 31
	v_lshl_add_u64 v[16:17], v[16:17], 0, s[0:1]
	v_cndmask_b32_e32 v23, v19, v23, vcc
	v_lshlrev_b32_e32 v33, 2, v23
	v_xor_b32_e32 v23, 16, v19
	v_cmp_lt_i32_e32 vcc, v23, v22
	s_lshl_b64 s[0:1], s[2:3], 11
	s_ashr_i32 s5, s4, 31
	v_cndmask_b32_e32 v23, v19, v23, vcc
	v_lshlrev_b32_e32 v34, 2, v23
	v_xor_b32_e32 v23, 32, v19
	v_cmp_lt_i32_e32 vcc, v23, v22
	v_lshl_or_b32 v18, v18, 3, s0
	s_lshl_b64 s[6:7], s[4:5], 11
	v_cndmask_b32_e32 v19, v19, v23, vcc
	v_lshlrev_b32_e32 v35, 2, v19
	v_mov_b32_e32 v19, s1
	s_lshl_b64 s[8:9], s[2:3], 4
	s_lshl_b64 s[10:11], s[4:5], 4
	s_lshl_b64 s[0:1], s[2:3], 12
	s_add_u32 s0, s82, s0
	s_addc_u32 s1, s83, s1
	v_lshl_add_u64 v[20:21], s[0:1], 0, v[20:21]
	s_mov_b64 s[0:1], 0xc00
	v_lshl_add_u64 v[20:21], v[20:21], 0, s[0:1]
	s_lshl_b64 s[12:13], s[4:5], 12
	v_mov_b32_e32 v36, 0x1500000
	s_mov_b32 s14, 0x3d800000
	v_mov_b32_e32 v37, 0x358637bd
	s_mov_b32 s3, 0xf800000
	v_mov_b32_e32 v38, 0x260
	v_mov_b32_e32 v23, 0x3d800000
	s_add_u32 s0, s92, s8
	s_addc_u32 s1, s93, s9
	global_load_dwordx4 v[120:123], v36, s[0:1]
	s_waitcnt vmcnt(0)
.LBB0_1286:
	s_add_u32 s0, s8, s10
	s_addc_u32 s1, s9, s11
	s_add_u32 s0, s0, s92
	s_addc_u32 s1, s1, s93
	v_lshl_add_u64 v[24:25], s[92:93], 0, v[18:19]
	s_waitcnt vmcnt(4)
	v_mov_b32_e32 v40, v120
	v_mov_b32_e32 v41, v121
	v_mov_b32_e32 v42, v122
	v_mov_b32_e32 v43, v123
	global_load_dwordx4 v[120:123], v36, s[0:1]
	v_add_co_u32_e32 v24, vcc, 0xe000000, v24
	v_mov_b32_e32 v27, v23
	s_nop 0
	v_addc_co_u32_e32 v25, vcc, 0, v25, vcc
	global_load_dwordx2 v[44:45], v[24:25], off offset:512
	global_load_dwordx2 v[46:47], v[24:25], off offset:1024
	global_load_dwordx2 v[48:49], v[24:25], off offset:1536
	global_load_dwordx2 v[50:51], v[24:25], off
	v_mov_b32_e32 v29, v23
	s_add_i32 s2, s2, s4
	s_add_u32 s8, s8, s10
	s_addc_u32 s9, s9, s11
	v_lshl_add_u64 v[18:19], v[18:19], 0, s[6:7]
	s_cmp_lt_i32 s2, 0x8000
	v_ashrrev_i32_e32 v25, 31, v40
	v_mov_b32_e32 v24, v40
	v_ashrrev_i32_e32 v53, 31, v41
	v_mov_b32_e32 v52, v41
	v_ashrrev_i32_e32 v41, 31, v42
	v_mov_b32_e32 v40, v42
	v_ashrrev_i32_e32 v55, 31, v43
	v_mov_b32_e32 v54, v43
	v_lshlrev_b64 v[24:25], 10, v[24:25]
	s_waitcnt vmcnt(1)
	v_lshlrev_b32_e32 v28, 16, v48
	v_and_b32_e32 v59, 0xffff0000, v48
	v_lshlrev_b32_e32 v43, 16, v49
	v_and_b32_e32 v57, 0xffff0000, v49
	v_lshlrev_b64 v[48:49], 10, v[52:53]
	v_lshlrev_b64 v[52:53], 10, v[54:55]
	v_lshlrev_b64 v[40:41], 10, v[40:41]
	v_lshl_add_u64 v[24:25], v[16:17], 0, v[24:25]
	v_lshl_add_u64 v[48:49], v[16:17], 0, v[48:49]
	v_lshl_add_u64 v[40:41], v[16:17], 0, v[40:41]
	v_lshl_add_u64 v[52:53], v[16:17], 0, v[52:53]
	global_load_dword v39, v[24:25], off
	global_load_dword v58, v[24:25], off offset:256
	global_load_dword v61, v[24:25], off offset:512
	global_load_dword v63, v[24:25], off offset:768
	global_load_dword v65, v[48:49], off
	global_load_dword v67, v[48:49], off offset:256
	global_load_dword v68, v[48:49], off offset:512
	global_load_dword v79, v[48:49], off offset:768
	global_load_dword v80, v[40:41], off
	global_load_dword v82, v[40:41], off offset:256
	global_load_dword v91, v[40:41], off offset:512
	global_load_dword v93, v[40:41], off offset:768
	global_load_dword v95, v[52:53], off
	global_load_dword v97, v[52:53], off offset:256
	global_load_dword v99, v[52:53], off offset:512
	global_load_dword v108, v[52:53], off offset:768
	s_waitcnt vmcnt(16)
	v_lshlrev_b32_e32 v54, 16, v50
	v_and_b32_e32 v55, 0xffff0000, v50
	v_lshlrev_b32_e32 v50, 16, v51
	v_and_b32_e32 v51, 0xffff0000, v51
	v_lshlrev_b32_e32 v22, 16, v44
	v_and_b32_e32 v26, 0xffff0000, v45
	v_lshlrev_b32_e32 v56, 16, v47
	v_lshlrev_b32_e32 v42, 16, v46
	v_and_b32_e32 v44, 0xffff0000, v44
	v_lshlrev_b32_e32 v45, 16, v45
	v_and_b32_e32 v47, 0xffff0000, v47
	v_and_b32_e32 v46, 0xffff0000, v46
	s_waitcnt vmcnt(15)
	v_cvt_f32_fp8_e32 v24, v39
	v_cvt_f32_fp8_sdwa v25, v39 src0_sel:BYTE_1
	v_cvt_f32_fp8_sdwa v40, v39 src0_sel:BYTE_2
	v_cvt_f32_fp8_sdwa v41, v39 src0_sel:BYTE_3
	s_waitcnt vmcnt(14)
	v_cvt_f32_fp8_e32 v48, v58
	v_cvt_f32_fp8_sdwa v52, v58 src0_sel:BYTE_1
	v_cvt_f32_fp8_sdwa v60, v58 src0_sel:BYTE_2
	v_cvt_f32_fp8_sdwa v62, v58 src0_sel:BYTE_3
	s_waitcnt vmcnt(13)
	v_cvt_f32_fp8_e32 v39, v61
	v_cvt_f32_fp8_sdwa v64, v61 src0_sel:BYTE_1
	v_cvt_f32_fp8_sdwa v58, v61 src0_sel:BYTE_2
	v_cvt_f32_fp8_sdwa v66, v61 src0_sel:BYTE_3
	s_waitcnt vmcnt(12)
	v_cvt_f32_fp8_e32 v110, v63
	v_cvt_f32_fp8_sdwa v69, v63 src0_sel:BYTE_1
	v_cvt_f32_fp8_sdwa v71, v63 src0_sel:BYTE_2
	v_cvt_f32_fp8_sdwa v73, v63 src0_sel:BYTE_3
	s_waitcnt vmcnt(10)
	v_cvt_f32_fp8_e32 v49, v67
	v_cvt_f32_fp8_sdwa v53, v67 src0_sel:BYTE_1
	v_cvt_f32_fp8_sdwa v61, v67 src0_sel:BYTE_2
	v_cvt_f32_fp8_sdwa v63, v67 src0_sel:BYTE_3
	v_cvt_f32_fp8_e32 v74, v65
	v_cvt_f32_fp8_sdwa v75, v65 src0_sel:BYTE_1
	v_cvt_f32_fp8_sdwa v76, v65 src0_sel:BYTE_2
	v_cvt_f32_fp8_sdwa v77, v65 src0_sel:BYTE_3
	s_waitcnt vmcnt(9)
	v_cvt_f32_fp8_e32 v70, v68
	v_cvt_f32_fp8_sdwa v65, v68 src0_sel:BYTE_1
	v_cvt_f32_fp8_sdwa v72, v68 src0_sel:BYTE_2
	v_cvt_f32_fp8_sdwa v67, v68 src0_sel:BYTE_3
	s_waitcnt vmcnt(8)
	v_cvt_f32_fp8_e32 v78, v79
	v_cvt_f32_fp8_sdwa v81, v79 src0_sel:BYTE_1
	v_cvt_f32_fp8_sdwa v83, v79 src0_sel:BYTE_2
	v_cvt_f32_fp8_sdwa v85, v79 src0_sel:BYTE_3
	s_waitcnt vmcnt(6)
	v_cvt_f32_fp8_e32 v68, v82
	v_cvt_f32_fp8_sdwa v90, v82 src0_sel:BYTE_1
	v_cvt_f32_fp8_sdwa v92, v82 src0_sel:BYTE_2
	v_cvt_f32_fp8_sdwa v94, v82 src0_sel:BYTE_3
	s_waitcnt vmcnt(5)
	v_cvt_f32_fp8_e32 v82, v91
	v_cvt_f32_fp8_sdwa v96, v91 src0_sel:BYTE_1
	v_cvt_f32_fp8_sdwa v84, v91 src0_sel:BYTE_2
	v_cvt_f32_fp8_sdwa v98, v91 src0_sel:BYTE_3
	s_waitcnt vmcnt(4)
	v_cvt_f32_fp8_e32 v79, v93
	v_cvt_f32_fp8_sdwa v112, v93 src0_sel:BYTE_1
	v_cvt_f32_fp8_sdwa v101, v93 src0_sel:BYTE_2
	v_cvt_f32_fp8_sdwa v103, v93 src0_sel:BYTE_3
	s_waitcnt vmcnt(2)
	v_cvt_f32_fp8_sdwa v91, v97 src0_sel:BYTE_1
	v_cvt_f32_fp8_sdwa v93, v97 src0_sel:BYTE_2
	v_cvt_f32_fp8_e32 v86, v80
	v_cvt_f32_fp8_sdwa v87, v80 src0_sel:BYTE_1
	v_cvt_f32_fp8_sdwa v88, v80 src0_sel:BYTE_2
	v_cvt_f32_fp8_sdwa v89, v80 src0_sel:BYTE_3
	v_cvt_f32_fp8_e32 v104, v95
	v_cvt_f32_fp8_sdwa v105, v95 src0_sel:BYTE_1
	v_cvt_f32_fp8_sdwa v106, v95 src0_sel:BYTE_2
	v_cvt_f32_fp8_sdwa v107, v95 src0_sel:BYTE_3
	v_cvt_f32_fp8_sdwa v95, v97 src0_sel:BYTE_3
	v_cvt_f32_fp8_e32 v80, v97
	s_waitcnt vmcnt(1)
	v_cvt_f32_fp8_e32 v100, v99
	v_cvt_f32_fp8_sdwa v97, v99 src0_sel:BYTE_1
	v_cvt_f32_fp8_sdwa v102, v99 src0_sel:BYTE_2
	v_cvt_f32_fp8_sdwa v99, v99 src0_sel:BYTE_3
	s_waitcnt vmcnt(0)
	v_cvt_f32_fp8_e32 v109, v108
	v_cvt_f32_fp8_sdwa v111, v108 src0_sel:BYTE_1
	v_cvt_f32_fp8_sdwa v114, v108 src0_sel:BYTE_2
	v_cvt_f32_fp8_sdwa v108, v108 src0_sel:BYTE_3
	v_pk_mul_f32 v[48:49], v[48:49], s[14:15] op_sel_hi:[1,0]
	v_pk_mul_f32 v[52:53], v[52:53], s[14:15] op_sel_hi:[1,0]
	v_pk_mul_f32 v[60:61], v[60:61], s[14:15] op_sel_hi:[1,0]
	v_pk_mul_f32 v[62:63], v[62:63], s[14:15] op_sel_hi:[1,0]
	v_pk_fma_f32 v[24:25], v[24:25], s[14:15], v[54:55] op_sel_hi:[1,0,1]
	v_pk_fma_f32 v[40:41], v[40:41], s[14:15], v[50:51] op_sel_hi:[1,0,1]
	v_fmac_f32_e32 v56, 0x3d800000, v58
	v_pk_mul_f32 v[64:65], v[64:65], s[14:15] op_sel_hi:[1,0]
	v_pk_mul_f32 v[66:67], v[66:67], s[14:15] op_sel_hi:[1,0]
	v_pk_mul_f32 v[50:51], v[90:91], s[14:15] op_sel_hi:[1,0]
	v_pk_mul_f32 v[54:55], v[92:93], s[14:15] op_sel_hi:[1,0]
	v_add_f32_e32 v22, v48, v22
	v_add_f32_e32 v26, v62, v26
	v_pk_fma_f32 v[24:25], v[74:75], s[14:15], v[24:25] op_sel_hi:[1,0,1]
	v_pk_fma_f32 v[40:41], v[76:77], s[14:15], v[40:41] op_sel_hi:[1,0,1]
	v_mov_b32_e32 v74, v52
	v_mov_b32_e32 v75, v60
	v_fmac_f32_e32 v42, 0x3d800000, v39
	v_fmac_f32_e32 v28, 0x3d800000, v110
	v_pk_mul_f32 v[78:79], v[78:79], s[14:15] op_sel_hi:[1,0]
	v_pk_mul_f32 v[90:91], v[94:95], s[14:15] op_sel_hi:[1,0]
	v_mov_b32_e32 v60, v53
	v_mov_b32_e32 v52, v50
	v_mov_b32_e32 v53, v54
	v_mov_b32_e32 v54, v51
	v_mov_b32_e32 v50, v64
	v_mov_b32_e32 v51, v66
	v_pk_fma_f32 v[56:57], v[72:73], s[14:15], v[56:57] op_sel_hi:[1,0,1]
	v_add_f32_e32 v58, v22, v49
	v_add_f32_e32 v22, v26, v63
	v_pk_fma_f32 v[24:25], v[86:87], s[14:15], v[24:25] op_sel_hi:[1,0,1]
	v_pk_fma_f32 v[40:41], v[88:89], s[14:15], v[40:41] op_sel_hi:[1,0,1]
	v_pk_add_f32 v[44:45], v[74:75], v[44:45]
	v_pk_mul_f32 v[92:93], v[96:97], s[14:15] op_sel_hi:[1,0]
	v_pk_mul_f32 v[94:95], v[98:99], s[14:15] op_sel_hi:[1,0]
	v_add_f32_e32 v28, v28, v78
	v_mov_b32_e32 v66, v65
	v_pk_fma_f32 v[42:43], v[70:71], s[14:15], v[42:43] op_sel_hi:[1,0,1]
	v_pk_add_f32 v[46:47], v[50:51], v[46:47]
	v_pk_fma_f32 v[50:51], v[84:85], s[14:15], v[56:57] op_sel_hi:[1,0,1]
	v_pk_fma_f32 v[24:25], v[104:105], s[14:15], v[24:25] op_sel_hi:[1,0,1]
	v_pk_fma_f32 v[40:41], v[106:107], s[14:15], v[40:41] op_sel_hi:[1,0,1]
	v_pk_add_f32 v[44:45], v[44:45], v[60:61]
	v_add_f32_e32 v22, v22, v90
	v_pk_fma_f32 v[56:57], v[68:69], s[14:15], v[58:59] op_sel_hi:[1,0,1]
	v_mul_f32_e32 v99, 0x3d800000, v108
	v_mov_b32_e32 v64, v92
	v_mov_b32_e32 v65, v94
	v_add_f32_e32 v49, v28, v79
	v_pk_fma_f32 v[42:43], v[82:83], s[14:15], v[42:43] op_sel_hi:[1,0,1]
	v_pk_add_f32 v[46:47], v[46:47], v[66:67]
	v_pk_add_f32 v[44:45], v[44:45], v[52:53]
	v_add_f32_e32 v116, v22, v91
	v_pk_mul_f32 v[52:53], v[40:41], v[40:41]
	v_pk_fma_f32 v[56:57], v[80:81], s[14:15], v[56:57] op_sel_hi:[1,0,1]
	v_mov_b32_e32 v108, v24
	v_mov_b32_e32 v22, v24
	v_mul_f32_e32 v48, v25, v25
	v_mul_f32_e32 v113, 0x3d800000, v112
	v_mul_f32_e32 v97, 0x3d800000, v114
	v_mov_b32_e32 v115, v109
	v_mov_b32_e32 v94, v93
	v_pk_fma_f32 v[42:43], v[100:101], s[14:15], v[42:43] op_sel_hi:[1,0,1]
	v_pk_fma_f32 v[50:51], v[102:103], s[14:15], v[50:51] op_sel_hi:[1,0,1]
	v_pk_add_f32 v[46:47], v[46:47], v[64:65]
	v_mov_b32_e32 v114, v40
	v_mov_b32_e32 v26, v40
	v_pk_add_f32 v[44:45], v[44:45], v[54:55]
	v_pk_fma_f32 v[54:55], v[108:109], v[22:23], v[48:49]
	v_mov_b32_e32 v48, v53
	v_mov_b32_e32 v112, v56
	v_mov_b32_e32 v96, v42
	v_mov_b32_e32 v98, v50
	v_pk_add_f32 v[46:47], v[46:47], v[94:95]
	v_pk_mul_f32 v[52:53], v[56:57], v[56:57]
	v_pk_mul_f32 v[64:65], v[44:45], v[44:45]
	v_pk_fma_f32 v[26:27], v[114:115], v[26:27], v[48:49]
	v_pk_add_f32 v[48:49], v[56:57], v[112:113]
	v_mov_b32_e32 v117, v111
	v_mov_b32_e32 v28, v116
	v_pk_add_f32 v[58:59], v[42:43], v[96:97]
	v_pk_add_f32 v[60:61], v[50:51], v[98:99]
	v_pk_mul_f32 v[66:67], v[46:47], v[46:47]
	v_mov_b32_e32 v110, v44
	v_mov_b32_e32 v22, v44
	v_mov_b32_e32 v53, v49
	v_mov_b32_e32 v48, v65
	v_pk_mul_f32 v[68:69], v[58:59], v[58:59]
	v_pk_mul_f32 v[70:71], v[60:61], v[60:61]
	v_mov_b32_e32 v57, v44
	v_mov_b32_e32 v62, v45
	v_mov_b32_e32 v60, v59
	v_pk_add_f32 v[44:45], v[54:55], v[26:27]
	v_pk_mul_f32 v[26:27], v[54:55], v[26:27]
	v_pk_fma_f32 v[58:59], v[42:43], v[42:43], v[66:67]
	v_pk_fma_f32 v[64:65], v[50:51], v[50:51], v[66:67] op_sel:[0,0,1] op_sel_hi:[1,1,0]
	v_mov_b32_e32 v43, v46
	v_mov_b32_e32 v51, v47
	v_pk_fma_f32 v[46:47], v[110:111], v[22:23], v[52:53]
	v_pk_fma_f32 v[28:29], v[116:117], v[28:29], v[48:49]
	v_mov_b32_e32 v45, v27
	v_pk_add_f32 v[26:27], v[46:47], v[28:29]
	v_pk_mul_f32 v[28:29], v[46:47], v[28:29]
	v_mov_b32_e32 v59, v69
	v_mov_b32_e32 v65, v71
	v_mov_b32_e32 v27, v29
	v_pk_add_f32 v[48:49], v[58:59], v[64:65]
	v_pk_add_f32 v[26:27], v[44:45], v[26:27]
	v_mov_b32_e32 v63, v116
	v_pk_add_f32 v[26:27], v[26:27], v[48:49]
	v_mov_b32_e32 v46, v55
	v_add_f32_e32 v22, v26, v27
	ds_bpermute_b32 v26, v30, v22
	s_waitcnt lgkmcnt(0)
	v_add_f32_e32 v22, v22, v26
	ds_bpermute_b32 v26, v31, v22
	s_waitcnt lgkmcnt(0)
	v_add_f32_e32 v22, v22, v26
	ds_bpermute_b32 v26, v32, v22
	s_waitcnt lgkmcnt(0)
	v_add_f32_e32 v22, v22, v26
	ds_bpermute_b32 v26, v33, v22
	s_waitcnt lgkmcnt(0)
	v_add_f32_e32 v22, v22, v26
	ds_bpermute_b32 v26, v34, v22
	s_waitcnt lgkmcnt(0)
	v_add_f32_e32 v22, v22, v26
	ds_bpermute_b32 v26, v35, v22
	s_waitcnt lgkmcnt(0)
	v_add_f32_e32 v22, v22, v26
	v_fmamk_f32 v22, v22, 0x3a800000, v37
	v_mul_f32_e32 v26, 0x4f800000, v22
	v_cmp_gt_f32_e32 vcc, s3, v22
	s_nop 1
	v_cndmask_b32_e32 v22, v22, v26, vcc
	v_sqrt_f32_e32 v26, v22
	s_nop 0
	v_add_u32_e32 v27, -1, v26
	v_add_u32_e32 v28, 1, v26
	v_fma_f32 v29, -v27, v26, v22
	v_fma_f32 v39, -v28, v26, v22
	v_cmp_ge_f32_e64 s[0:1], 0, v29
	s_nop 1
	v_cndmask_b32_e64 v26, v26, v27, s[0:1]
	v_cmp_lt_f32_e64 s[0:1], 0, v39
	s_nop 1
	v_cndmask_b32_e64 v26, v26, v28, s[0:1]
	v_mul_f32_e32 v27, 0x37800000, v26
	v_cndmask_b32_e32 v26, v26, v27, vcc
	v_cmp_class_f32_e32 vcc, v22, v38
	s_nop 1
	v_cndmask_b32_e32 v22, v26, v22, vcc
	v_div_scale_f32 v26, s[0:1], v22, v22, 1.0
	v_rcp_f32_e32 v28, v26
	v_div_scale_f32 v27, vcc, 1.0, v22, 1.0
	v_fma_f32 v29, -v26, v28, 1.0
	v_fmac_f32_e32 v28, v29, v28
	v_mul_f32_e32 v29, v27, v28
	v_fma_f32 v39, -v26, v29, v27
	v_fmac_f32_e32 v29, v39, v28
	v_fma_f32 v26, -v26, v29, v27
	v_div_fmas_f32 v26, v26, v28, v29
	v_div_fixup_f32 v22, v26, v22, 1.0
	v_pk_mul_f32 v[24:25], v[24:25], v[22:23] op_sel_hi:[1,0]
	v_pk_mul_f32 v[26:27], v[40:41], v[22:23] op_sel_hi:[1,0]
	v_pk_mul_f32 v[28:29], v[56:57], v[22:23] op_sel_hi:[1,0]
	v_pk_mul_f32 v[40:41], v[62:63], v[22:23] op_sel_hi:[1,0]
	v_pk_mul_f32 v[44:45], v[42:43], v[22:23] op_sel_hi:[1,0]
	v_pk_mul_f32 v[48:49], v[50:51], v[22:23] op_sel_hi:[1,0]
	v_pk_mul_f32 v[52:53], v[46:47], v[22:23] op_sel_hi:[1,0]
	v_pk_mul_f32 v[50:51], v[60:61], v[22:23] op_sel_hi:[1,0]
	v_pk_mul_f32 v[26:27], v[2:3], v[26:27]
	v_pk_mul_f32 v[24:25], v[0:1], v[24:25]
	v_pk_mul_f32 v[42:43], v[6:7], v[40:41]
	v_pk_mul_f32 v[40:41], v[4:5], v[28:29]
	v_pk_mul_f32 v[46:47], v[10:11], v[48:49]
	v_pk_mul_f32 v[44:45], v[8:9], v[44:45]
	v_pk_mul_f32 v[50:51], v[14:15], v[50:51]
	v_pk_mul_f32 v[48:49], v[12:13], v[52:53]
	global_store_dwordx4 v[20:21], v[24:27], off offset:-3072 nt
	global_store_dwordx4 v[20:21], v[40:43], off offset:-2048 nt
	global_store_dwordx4 v[20:21], v[44:47], off offset:-1024 nt
	global_store_dwordx4 v[20:21], v[48:51], off nt
	v_lshl_add_u64 v[20:21], v[20:21], 0, s[12:13]
	s_cbranch_scc1 .LBB0_1286
